# speedup vs baseline: 1.0370x; 1.0370x over previous
.LBB2_23:
	s_or_b64 exec, exec, s[12:13]
	s_waitcnt lgkmcnt(1)
	v_mov_b32_e32 v136, 0
	s_waitcnt lgkmcnt(0)
	s_barrier
	ds_read_b128 v[2:5], v136
	ds_read_b128 v[136:139], v136 offset:16
	s_mov_b32 s12, 0x800000
	s_waitcnt lgkmcnt(1)
	v_max_f32_e32 v140, v5, v5
	v_max_f32_e32 v141, v4, v4
	v_max_f32_e32 v140, v141, v140
	v_max3_f32 v140, v2, v3, v140
	v_sub_f32_e32 v2, v2, v140
	v_sub_f32_e32 v3, v3, v140
	v_mul_f32_e32 v2, 0x3fb8aa3b, v2
	v_mul_f32_e32 v3, 0x3fb8aa3b, v3
	v_sub_f32_e32 v4, v4, v140
	v_sub_f32_e32 v5, v5, v140
	v_exp_f32_e32 v2, v2
	v_exp_f32_e32 v3, v3
	v_mul_f32_e32 v4, 0x3fb8aa3b, v4
	v_mul_f32_e32 v5, 0x3fb8aa3b, v5
	v_exp_f32_e32 v4, v4
	v_exp_f32_e32 v5, v5
	s_waitcnt lgkmcnt(0)
	v_pk_mul_f32 v[2:3], v[136:137], v[2:3]
	v_pk_mul_f32 v[4:5], v[138:139], v[4:5]
	v_add_f32_e32 v2, v2, v3
	v_add_f32_e32 v2, v4, v2
	v_add_f32_e32 v2, v5, v2
	v_cmp_gt_f32_e32 vcc, s12, v2
	s_and_b64 s[12:13], vcc, exec
	s_cselect_b32 s12, 32, 0
	v_ldexp_f32 v2, v2, s12
	v_log_f32_e32 v2, v2
	s_mov_b32 s12, 0x3f317217
	v_mov_b32_e32 v3, 0x41b17218
	v_cndmask_b32_e32 v3, 0, v3, vcc
	v_mul_f32_e32 v5, 0x3f317217, v2
	v_fma_f32 v5, v2, s12, -v5
	v_fmamk_f32 v5, v2, 0x3377d1cf, v5
	s_mov_b32 s12, 0x7f800000
	v_fmac_f32_e32 v5, 0x3f317217, v2
	v_cmp_lt_f32_e64 vcc, |v2|, s12
	s_lshl_b64 s[10:11], s[10:11], 2
	v_lshlrev_b32_e32 v4, 5, v0
	v_cndmask_b32_e32 v2, v2, v5, vcc
	v_sub_f32_e32 v2, v2, v3
	v_add_f32_e32 v2, v140, v2
	s_add_u32 s0, s0, s10
	s_addc_u32 s1, s1, s11
	v_sub_f32_e32 v139, v133, v2
	v_sub_f32_e32 v138, v132, v2
	v_sub_f32_e32 v137, v126, v2
	v_sub_f32_e32 v136, v124, v2
	v_sub_f32_e32 v127, v127, v2
	v_sub_f32_e32 v126, v125, v2
	v_sub_f32_e32 v125, v120, v2
	v_sub_f32_e32 v124, v117, v2
	v_or_b32_e32 v3, 0x2000, v4
	v_sub_f32_e32 v135, v135, v2
	v_sub_f32_e32 v134, v134, v2
	v_sub_f32_e32 v133, v131, v2
	v_sub_f32_e32 v132, v129, v2
	global_store_dwordx4 v4, v[136:139], s[0:1]
	global_store_dwordx4 v4, v[132:135], s[0:1] offset:16
	v_sub_f32_e32 v131, v130, v2
	v_sub_f32_e32 v130, v128, v2
	v_sub_f32_e32 v129, v123, v2
	v_sub_f32_e32 v128, v121, v2
	global_store_dwordx4 v3, v[124:127], s[0:1]
	global_store_dwordx4 v3, v[128:131], s[0:1] offset:16
	v_sub_f32_e32 v120, v119, v2
	v_sub_f32_e32 v127, v118, v2
	v_sub_f32_e32 v126, v116, v2
	v_sub_f32_e32 v125, v112, v2
	v_sub_f32_e32 v124, v109, v2
	v_sub_f32_e32 v119, v115, v2
	v_sub_f32_e32 v118, v113, v2
	v_or_b32_e32 v3, 0x4000, v4
	v_sub_f32_e32 v121, v122, v2
	global_store_dwordx4 v3, v[124:127], s[0:1]
	global_store_dwordx4 v3, v[118:121], s[0:1] offset:16
	v_sub_f32_e32 v117, v104, v2
	v_sub_f32_e32 v116, v101, v2
	v_sub_f32_e32 v119, v110, v2
	v_sub_f32_e32 v118, v108, v2
	v_sub_f32_e32 v112, v111, v2
	v_sub_f32_e32 v111, v107, v2
	v_sub_f32_e32 v110, v105, v2
	v_or_b32_e32 v3, 0x6000, v4
	v_sub_f32_e32 v113, v114, v2
	global_store_dwordx4 v3, v[116:119], s[0:1]
	global_store_dwordx4 v3, v[110:113], s[0:1] offset:16
	v_sub_f32_e32 v109, v96, v2
	v_sub_f32_e32 v108, v93, v2
	v_sub_f32_e32 v111, v102, v2
	v_sub_f32_e32 v110, v100, v2
	v_sub_f32_e32 v104, v103, v2
	v_sub_f32_e32 v103, v99, v2
	v_sub_f32_e32 v102, v97, v2
	v_lshlrev_b32_e32 v3, 5, v71
	v_sub_f32_e32 v105, v106, v2
	global_store_dwordx4 v3, v[108:111], s[0:1]
	global_store_dwordx4 v3, v[102:105], s[0:1] offset:16
	v_sub_f32_e32 v101, v88, v2
	v_sub_f32_e32 v100, v85, v2
	v_sub_f32_e32 v103, v94, v2
	v_sub_f32_e32 v102, v92, v2
	v_sub_f32_e32 v96, v95, v2
	v_sub_f32_e32 v95, v91, v2
	v_sub_f32_e32 v94, v89, v2
	v_or_b32_e32 v3, 0xa000, v4
	v_sub_f32_e32 v97, v98, v2
	global_store_dwordx4 v3, v[100:103], s[0:1]
	global_store_dwordx4 v3, v[94:97], s[0:1] offset:16
	v_sub_f32_e32 v93, v72, v2
	v_sub_f32_e32 v92, v63, v2
	v_sub_f32_e32 v95, v86, v2
	v_sub_f32_e32 v94, v80, v2
	v_sub_f32_e32 v89, v90, v2
	v_sub_f32_e32 v88, v87, v2
	v_sub_f32_e32 v87, v79, v2
	v_sub_f32_e32 v86, v73, v2
	v_or_b32_e32 v3, 0xc000, v4
	global_store_dwordx4 v3, v[92:95], s[0:1]
	global_store_dwordx4 v3, v[86:89], s[0:1] offset:16
	v_or_b32_e32 v3, 0xe000, v4
	v_sub_f32_e32 v93, v74, v2
	v_sub_f32_e32 v89, v64, v2
	v_sub_f32_e32 v88, v60, v2
	v_sub_f32_e32 v87, v54, v2
	v_sub_f32_e32 v86, v51, v2
	v_sub_f32_e32 v92, v65, v2
	v_sub_f32_e32 v91, v57, v2
	v_sub_f32_e32 v90, v55, v2
	global_store_dwordx4 v3, v[86:89], s[0:1]
	global_store_dwordx4 v3, v[90:93], s[0:1] offset:16
	v_sub_f32_e32 v54, v53, v2
	v_sub_f32_e32 v89, v52, v2
	v_sub_f32_e32 v88, v50, v2
	v_sub_f32_e32 v87, v46, v2
	v_sub_f32_e32 v86, v43, v2
	v_sub_f32_e32 v53, v49, v2
	v_sub_f32_e32 v52, v47, v2
	v_lshlrev_b32_e32 v3, 5, v70
	v_sub_f32_e32 v55, v56, v2
	global_store_dwordx4 v3, v[86:89], s[0:1]
	global_store_dwordx4 v3, v[52:55], s[0:1] offset:16
	v_sub_f32_e32 v51, v38, v2
	v_sub_f32_e32 v50, v35, v2
	v_sub_f32_e32 v53, v44, v2
	v_sub_f32_e32 v52, v42, v2
	v_sub_f32_e32 v46, v45, v2
	v_sub_f32_e32 v45, v41, v2
	v_sub_f32_e32 v44, v39, v2
	v_or_b32_e32 v3, 0x12000, v4
	v_sub_f32_e32 v47, v48, v2
	global_store_dwordx4 v3, v[50:53], s[0:1]
	global_store_dwordx4 v3, v[44:47], s[0:1] offset:16
	v_sub_f32_e32 v43, v30, v2
	v_sub_f32_e32 v42, v27, v2
	v_sub_f32_e32 v45, v36, v2
	v_sub_f32_e32 v44, v34, v2
	v_sub_f32_e32 v38, v37, v2
	v_sub_f32_e32 v37, v33, v2
	v_sub_f32_e32 v36, v31, v2
	v_or_b32_e32 v3, 0x14000, v4
	v_sub_f32_e32 v39, v40, v2
	global_store_dwordx4 v3, v[42:45], s[0:1]
	global_store_dwordx4 v3, v[36:39], s[0:1] offset:16
	v_sub_f32_e32 v35, v23, v2
	v_sub_f32_e32 v34, v22, v2
	v_sub_f32_e32 v37, v28, v2
	v_sub_f32_e32 v36, v26, v2
	v_or_b32_e32 v3, 0x16000, v4
	v_sub_f32_e32 v27, v32, v2
	v_sub_f32_e32 v26, v29, v2
	v_sub_f32_e32 v25, v25, v2
	v_sub_f32_e32 v24, v24, v2
	global_store_dwordx4 v3, v[34:37], s[0:1]
	global_store_dwordx4 v3, v[24:27], s[0:1] offset:16
	s_and_saveexec_b64 s[10:11], s[8:9]
	s_cbranch_execnz .LBB2_31
	s_or_b64 exec, exec, s[10:11]
	s_and_saveexec_b64 s[8:9], s[2:3]
	s_cbranch_execnz .LBB2_32

.LBB2_31:
	v_sub_f32_e32 v24, v20, v2
	v_sub_f32_e32 v22, v18, v2
	v_sub_f32_e32 v25, v19, v2
	v_sub_f32_e32 v23, v6, v2
	v_lshlrev_b32_e32 v1, 5, v1
	v_sub_f32_e32 v20, v21, v2
	v_sub_f32_e32 v18, v15, v2
	v_sub_f32_e32 v21, v16, v2
	v_sub_f32_e32 v19, v14, v2
	global_store_dwordx4 v1, v[22:25], s[0:1]
	global_store_dwordx4 v1, v[18:21], s[0:1] offset:16
	s_or_b64 exec, exec, s[10:11]
	s_and_saveexec_b64 s[8:9], s[2:3]
	s_cbranch_execz .LBB2_25
.LBB2_32:
	v_mov_b32_e32 v1, 0x1a000
	v_sub_f32_e32 v20, v83, v2
	v_sub_f32_e32 v18, v77, v2
	v_sub_f32_e32 v21, v81, v2
	v_sub_f32_e32 v19, v75, v2
	v_lshl_or_b32 v1, v0, 5, v1
	v_sub_f32_e32 v24, v84, v2
	v_sub_f32_e32 v22, v78, v2
	v_sub_f32_e32 v25, v82, v2
	v_sub_f32_e32 v23, v76, v2
	global_store_dwordx4 v1, v[18:21], s[0:1]
	global_store_dwordx4 v1, v[22:25], s[0:1] offset:16
	s_or_b64 exec, exec, s[8:9]
	s_and_saveexec_b64 s[2:3], s[4:5]
	s_cbranch_execz .LBB2_26
.LBB2_33:
	v_mov_b32_e32 v1, 0x1c000
	v_sub_f32_e32 v20, v68, v2
	v_sub_f32_e32 v18, v61, v2
	v_sub_f32_e32 v21, v66, v2
	v_sub_f32_e32 v19, v58, v2
	v_lshl_or_b32 v1, v0, 5, v1
	v_sub_f32_e32 v24, v69, v2
	v_sub_f32_e32 v22, v62, v2
	v_sub_f32_e32 v25, v67, v2
	v_sub_f32_e32 v23, v59, v2
	global_store_dwordx4 v1, v[18:21], s[0:1]
	global_store_dwordx4 v1, v[22:25], s[0:1] offset:16
	s_or_b64 exec, exec, s[2:3]
	s_and_saveexec_b64 s[2:3], s[6:7]
	s_cbranch_execz .LBB2_27
.LBB2_34:
	v_mov_b32_e32 v1, 0x1e000
	v_sub_f32_e32 v20, v13, v2
	v_sub_f32_e32 v18, v9, v2
	v_sub_f32_e32 v21, v11, v2
	v_sub_f32_e32 v19, v7, v2
	v_lshl_or_b32 v0, v0, 5, v1
	v_sub_f32_e32 v6, v17, v2
	v_sub_f32_e32 v4, v10, v2
	v_sub_f32_e32 v7, v12, v2
	v_sub_f32_e32 v5, v8, v2
	global_store_dwordx4 v0, v[18:21], s[0:1]
	global_store_dwordx4 v0, v[4:7], s[0:1] offset:16
	s_endpgm
	s_nop 0
	s_nop 0
	s_nop 0
	s_nop 0
	s_nop 0
	s_nop 0
	s_nop 0
	s_nop 0
	s_nop 0
	s_nop 0
	s_nop 0
	s_nop 0
	s_nop 0
	s_nop 0
	s_nop 0
	s_nop 0
	s_nop 0
	s_nop 0
	s_nop 0
	s_nop 0
	s_nop 0
	s_nop 0
	s_nop 0
	s_nop 0
	s_nop 0
	s_nop 0
	s_nop 0
	s_nop 0
	s_nop 0
	s_nop 0
	s_nop 0
	s_nop 0
	s_nop 0
	s_nop 0
	s_nop 0
	s_nop 0
	s_nop 0
	s_nop 0
	s_nop 0
	s_nop 0
	s_nop 0
	s_nop 0
	s_nop 0
	s_nop 0
	s_nop 0
	s_nop 0
	s_nop 0
	s_endpgm
